# s13p + attention work queue: fetch-add for the next block index issued at the start of the current block's epilogue (late look-ahead), pop only waits and publishes; L0 and L1; padded
# baseline (speedup 1.0000x reference)
; DI float wave_sum(float v) { v += shx<1>(v); v += shx<2>(v); v += shx<4>(v); v += shx<8>(v); v += shx<16>(v); v += shx<32>(v); return v; }
; template <int L> DI void layer_phases(const Params& P, Frame& F, const XcdBarrier& bar, int lo, int hi) {
;     ...
;             const float li = (L == 0) ? 0.2f : 0.35550906759f;
;             const float d1 = wave_sum(P.in[I_LQ1][L * 64 + F.lane] * P.in[I_LK1][L * 64 + F.lane]), d2 = wave_sum(P.in[I_LQ2][L * 64 + F.lane] * P.in[I_LK2][L * 64 + F.lane]);
;             const float lam = __expf(d1) - __expf(d2) + li;
;             unsigned* qctr = (unsigned*)(ws + WS_CTL) + CW_QUEUE + 64 * L;
;             for (;;) {
;                 __syncthreads();
;                 if (F.tid == 0) F.MISC[24] = __hip_atomic_fetch_add(qctr, 1u, __ATOMIC_RELAXED, __HIP_MEMORY_SCOPE_AGENT);
.LBB0_1045:
	v_ashrrev_i32_e32 v137, 31, v136
	s_waitcnt lgkmcnt(0)
	v_readlane_b32 s4, v254, 5
	v_lshlrev_b64 v[0:1], 2, v[136:137]
	v_readlane_b32 s6, v254, 7
	v_readlane_b32 s7, v254, 8
	v_readlane_b32 s8, v254, 9
	v_readlane_b32 s9, v254, 10
	v_lshl_add_u64 v[2:3], s[6:7], 0, v[0:1]
	v_readlane_b32 s10, v254, 11
	v_readlane_b32 s11, v254, 12
	v_readlane_b32 s12, v254, 13
	v_readlane_b32 s13, v254, 14
	global_load_dword v4, v[2:3], off
	v_lshl_add_u64 v[2:3], s[8:9], 0, v[0:1]
	global_load_dword v5, v[2:3], off
	v_lshl_add_u64 v[2:3], s[10:11], 0, v[0:1]
	v_lshl_add_u64 v[0:1], s[12:13], 0, v[0:1]
	global_load_dword v2, v[2:3], off
	v_xor_b32_e32 v3, 32, v193
	global_load_dword v1, v[0:1], off
	v_and_b32_e32 v0, 64, v193
	v_add_u32_e32 v12, 64, v0
	v_ashrrev_i32_e32 v6, 4, v136
	v_cmp_lt_i32_e32 vcc, v3, v12
	v_add_u32_e32 v8, 0x200, v138
	v_bfe_u32 v9, v136, 3, 1
	s_movk_i32 s6, 0x2400
	v_bfe_u32 v11, v136, 2, 2
	v_lshlrev_b32_e32 v130, 2, v6
	v_cndmask_b32_e32 v3, v193, v3, vcc
	v_ashrrev_i32_e32 v128, 4, v8
	v_mul_u32_u24_e32 v182, 0x2400, v9
	v_mad_u32_u24 v8, v9, s6, 0
	v_or_b32_e32 v9, v130, v11
	v_lshlrev_b32_e32 v190, 2, v3
	v_lshlrev_b32_e32 v7, 3, v136
	v_ashrrev_i32_e32 v114, 4, v138
	s_movk_i32 s7, 0x90
	s_movk_i32 s8, 0x110
	v_and_b32_e32 v0, 24, v7
	v_mul_lo_u32 v183, v114, s7
	v_mul_lo_u32 v188, v128, s7
	s_add_u32 s0, s54, 0x2000
	s_addc_u32 s1, s55, 0
	v_lshlrev_b32_e32 v10, 4, v136
	s_add_u32 s58, s54, 0x41600000
	v_and_b32_e32 v127, 15, v136
	v_lshlrev_b32_e32 v124, 3, v6
	v_and_b32_e32 v184, 0x70, v10
	v_add_u32_e32 v6, v8, v183
	s_addc_u32 s59, s55, 0
	s_lshl_b32 s64, s86, 4
	v_mul_lo_u32 v185, v114, s8
	v_mul_lo_u32 v189, v128, s8
	v_sub_u32_e32 v10, v130, v127
	v_readlane_b32 s5, v254, 6
	v_readlane_b32 s14, v254, 15
	v_readlane_b32 s15, v254, 16
	v_and_b32_e32 v126, 0x78, v7
	v_lshlrev_b32_e32 v186, 4, v127
	v_add_u32_e32 v7, 0, v185
	v_ashrrev_i32_e32 v131, 31, v130
	s_mov_b32 s39, 0
	v_cmp_eq_u32_e64 s[4:5], 0, v138
	v_mov_b32_e32 v113, 0
	v_and_b32_e32 v161, -16, v136
	s_movk_i32 s3, 0x3800
	s_mov_b32 s56, 0x3e38aa3b
	s_movk_i32 s33, 0x2000
	s_mov_b32 s57, 0xff800000
	v_mov_b32_e32 v179, 0x358637bd
	v_mov_b32_e32 v180, 0x42800000
	v_mov_b32_e32 v181, 0x3fb8aa3b
	v_mov_b32_e32 v116, 2.0
	v_mov_b32_e32 v117, 0x40400000
	v_mov_b32_e32 v118, 0x41800000
	v_mov_b32_e32 v119, 0x41880000
	v_mov_b32_e32 v120, 0x41900000
	v_mov_b32_e32 v121, 0x41980000
	v_mov_b32_e32 v122, 0x42000000
	v_mov_b32_e32 v123, 0x42040000
	v_ashrrev_i32_e32 v115, 31, v114
	v_mul_u32_u24_e32 v187, 0x90, v127
	v_ashrrev_i32_e32 v125, 31, v124
	v_ashrrev_i32_e32 v129, 31, v128
	v_lshl_add_u64 v[134:135], v[130:131], 2, s[14:15]
	s_add_i32 s65, 0, 0x22060
	v_add_u32_e32 v191, v7, v186
	v_mov_b32_e32 v136, 0x42080000
	v_mov_b32_e32 v137, 0x420c0000
	v_mov_b32_e32 v138, 0x42400000
	v_mov_b32_e32 v139, 0x42440000
	v_mov_b32_e32 v140, 0x42480000
	v_mov_b32_e32 v141, 0x424c0000
	s_waitcnt vmcnt(2)
	v_mul_f32_e32 v3, v4, v5
	v_mov_b32_e32 v198, 0xff800000
	v_readlane_b32 s16, v254, 17
	v_mov_b32_dpp v3, v3 quad_perm:[1,0,3,2] row_mask:0xf bank_mask:0xf bound_ctrl:1
	v_fmac_f32_e32 v3, v4, v5
	s_waitcnt vmcnt(0)
	v_mul_f32_e32 v11, v2, v1
	v_add_u32_e32 v5, v8, v188
	v_add_u32_e32 v8, 0, v189
	v_mov_b32_dpp v11, v11 quad_perm:[1,0,3,2] row_mask:0xf bank_mask:0xf bound_ctrl:1
	v_fmac_f32_e32 v11, v2, v1
	v_add_f32_dpp v1, v3, v3 quad_perm:[2,3,0,1] row_mask:0xf bank_mask:0xf bound_ctrl:1
	ds_swizzle_b32 v3, v1 offset:swizzle(SWAP,4)
	v_add_f32_dpp v2, v11, v11 quad_perm:[2,3,0,1] row_mask:0xf bank_mask:0xf bound_ctrl:1
	ds_swizzle_b32 v4, v2 offset:swizzle(SWAP,4)
	v_add_u32_e32 v193, v5, v184
	v_add_u32_e32 v194, v8, v186
	s_waitcnt lgkmcnt(1)
	v_add_f32_e32 v1, v1, v3
	ds_swizzle_b32 v3, v1 offset:swizzle(SWAP,8)
	s_waitcnt lgkmcnt(1)
	v_add_f32_e32 v2, v2, v4
	ds_swizzle_b32 v4, v2 offset:swizzle(SWAP,8)
	v_mad_u64_u32 v[132:133], s[6:7], v9, s8, v[0:1]
	s_waitcnt lgkmcnt(1)
	v_add_f32_e32 v0, v1, v3
	v_add_u32_e32 v133, v6, v184
	s_waitcnt lgkmcnt(0)
	v_add_f32_e32 v1, v2, v4
	ds_swizzle_b32 v2, v0 offset:swizzle(SWAP,16)
	ds_swizzle_b32 v3, v1 offset:swizzle(SWAP,16)
	v_or_b32_e32 v6, s64, v127
	v_subrev_u32_e32 v4, s64, v10
	v_add_u32_e32 v195, 64, v4
	s_waitcnt lgkmcnt(1)
	v_add_f32_e32 v0, v0, v2
	s_waitcnt lgkmcnt(0)
	v_add_f32_e32 v1, v1, v3
	ds_bpermute_b32 v2, v190, v0
	ds_bpermute_b32 v3, v190, v1
	v_readlane_b32 s17, v254, 18
	v_readlane_b32 s18, v254, 19
	v_readlane_b32 s19, v254, 20
	s_waitcnt lgkmcnt(1)
	v_add_f32_e32 v0, v0, v2
	s_waitcnt lgkmcnt(0)
	v_add_f32_e32 v1, v1, v3
	v_mul_f32_e32 v0, 0x3fb8aa3b, v0
	v_mul_f32_e32 v1, 0x3fb8aa3b, v1
	v_exp_f32_e32 v0, v0
	v_exp_f32_e32 v1, v1
	v_sub_u32_e32 v2, v6, v130
	v_subrev_u32_e32 v196, 64, v2
	v_sub_f32_e32 v0, v0, v1
	v_add_f32_e32 v197, 0x3e4ccccd, v0
	s_mov_b64 s[6:7], exec
	s_and_b64 exec, exec, s[4:5]
	v_mov_b32_e32 v252, 1
	global_atomic_add v252, v113, v252, s[0:1] sc0
	s_mov_b64 exec, s[6:7]
	s_branch .LBB0_1048
; DI void attn_block(const Params& P, const Frame& F, int L, int b, int h, int qb, float lam, float oml) {
;     ...
;     const float* nw = P.in[I_DIFF_NORM] + L * 128;
;     f32x4 nwv[8];
; #pragma unroll
;     for (int d = 0; d < 8; ++d) nwv[d] = *(const f32x4*)(nw + 16 * d + 4 * rq);
;     float inv[2];
; #pragma unroll
;     for (int j = 0; j < 2; ++j) { float l = lrun[j]; l += shx<16>(l); l += shx<32>(l); inv[j] = __builtin_amdgcn_rcpf(l); }
;     const float inv1l = lam * inv[1];
;     float ss = 0.f;
; #pragma unroll
;     for (int d = 0; d < 8; ++d)
; #pragma unroll
;         for (int e = 0; e < 4; ++e) { const float o = O[0][d][e] * inv[0] - O[1][d][e] * inv1l; O[0][d][e] = o; ss += o * o; }
;     ss += shx<16>(ss); ss += shx<32>(ss);
.LBB0_1046:
	s_mov_b64 s[6:7], exec
	s_and_b64 exec, exec, s[4:5]
	v_mov_b32_e32 v252, 1
	global_atomic_add v252, v113, v252, s[0:1] sc0
	s_mov_b64 exec, s[6:7]
	global_load_dwordx4 v[0:3], v[134:135], off
	global_load_dwordx4 v[4:7], v[134:135], off offset:64
	ds_swizzle_b32 v8, v203 offset:swizzle(SWAP,16)
	ds_swizzle_b32 v9, v204 offset:swizzle(SWAP,16)
	s_lshl_b32 s38, s66, 1
	s_mov_b64 s[6:7], 0x61400400
	v_readlane_b32 s68, v254, 37
	s_waitcnt lgkmcnt(1)
	v_add_f32_e32 v24, v203, v8
	s_waitcnt lgkmcnt(0)
	v_add_f32_e32 v25, v204, v9
	ds_bpermute_b32 v26, v190, v24
	ds_bpermute_b32 v27, v190, v25
	global_load_dwordx4 v[8:11], v[134:135], off offset:128
	global_load_dwordx4 v[12:15], v[134:135], off offset:192
	global_load_dwordx4 v[16:19], v[134:135], off offset:256
	global_load_dwordx4 v[20:23], v[134:135], off offset:320
	v_readlane_b32 s70, v254, 39
	v_readlane_b32 s71, v254, 40
	s_waitcnt lgkmcnt(1)
	v_add_f32_e32 v24, v24, v26
	s_waitcnt lgkmcnt(0)
	v_add_f32_e32 v25, v25, v27
	v_rcp_f32_e32 v97, v25
	v_rcp_f32_e32 v96, v24
	global_load_dwordx4 v[24:27], v[134:135], off offset:384
	global_load_dwordx4 v[28:31], v[134:135], off offset:448
	v_readlane_b32 s72, v254, 41
	v_mul_f32_e32 v98, v197, v97
	v_pk_mul_f32 v[36:37], v[36:37], v[98:99] op_sel_hi:[1,0]
	v_pk_mul_f32 v[38:39], v[38:39], v[98:99] op_sel_hi:[1,0]
	v_pk_fma_f32 v[32:33], v[32:33], v[96:97], v[36:37] op_sel_hi:[1,0,1] neg_lo:[0,0,1] neg_hi:[0,0,1]
	v_pk_fma_f32 v[34:35], v[34:35], v[96:97], v[38:39] op_sel_hi:[1,0,1] neg_lo:[0,0,1] neg_hi:[0,0,1]
	v_pk_mul_f32 v[36:37], v[32:33], v[32:33]
	v_pk_mul_f32 v[56:57], v[56:57], v[98:99] op_sel_hi:[1,0]
	v_pk_mul_f32 v[38:39], v[34:35], v[34:35]
	v_add_f32_e32 v36, v36, v37
	v_pk_fma_f32 v[40:41], v[40:41], v[96:97], v[56:57] op_sel_hi:[1,0,1] neg_lo:[0,0,1] neg_hi:[0,0,1]
	v_add_f32_e32 v36, v38, v36
	v_pk_mul_f32 v[58:59], v[58:59], v[98:99] op_sel_hi:[1,0]
	v_pk_mul_f32 v[56:57], v[40:41], v[40:41]
	v_add_f32_e32 v36, v39, v36
	v_pk_fma_f32 v[42:43], v[42:43], v[96:97], v[58:59] op_sel_hi:[1,0,1] neg_lo:[0,0,1] neg_hi:[0,0,1]
	v_add_f32_e32 v36, v56, v36
	v_pk_mul_f32 v[80:81], v[80:81], v[98:99] op_sel_hi:[1,0]
	v_pk_mul_f32 v[58:59], v[42:43], v[42:43]
	v_add_f32_e32 v36, v57, v36
	v_pk_fma_f32 v[60:61], v[60:61], v[96:97], v[80:81] op_sel_hi:[1,0,1] neg_lo:[0,0,1] neg_hi:[0,0,1]
	v_add_f32_e32 v36, v58, v36
	v_pk_mul_f32 v[82:83], v[82:83], v[98:99] op_sel_hi:[1,0]
	v_pk_mul_f32 v[80:81], v[60:61], v[60:61]
	v_add_f32_e32 v36, v59, v36
	v_pk_fma_f32 v[62:63], v[62:63], v[96:97], v[82:83] op_sel_hi:[1,0,1] neg_lo:[0,0,1] neg_hi:[0,0,1]
	v_add_f32_e32 v36, v80, v36
	v_pk_mul_f32 v[64:65], v[64:65], v[98:99] op_sel_hi:[1,0]
	v_pk_mul_f32 v[82:83], v[62:63], v[62:63]
	v_add_f32_e32 v36, v81, v36
	v_pk_fma_f32 v[64:65], v[68:69], v[96:97], v[64:65] op_sel_hi:[1,0,1] neg_lo:[0,0,1] neg_hi:[0,0,1]
	v_add_f32_e32 v36, v82, v36
	v_pk_mul_f32 v[66:67], v[66:67], v[98:99] op_sel_hi:[1,0]
	v_pk_mul_f32 v[68:69], v[64:65], v[64:65]
	v_add_f32_e32 v36, v83, v36
	v_pk_fma_f32 v[66:67], v[70:71], v[96:97], v[66:67] op_sel_hi:[1,0,1] neg_lo:[0,0,1] neg_hi:[0,0,1]
	v_add_f32_e32 v36, v68, v36
	v_pk_mul_f32 v[48:49], v[48:49], v[98:99] op_sel_hi:[1,0]
	v_pk_mul_f32 v[70:71], v[66:67], v[66:67]
	v_add_f32_e32 v36, v69, v36
	v_pk_fma_f32 v[44:45], v[44:45], v[96:97], v[48:49] op_sel_hi:[1,0,1] neg_lo:[0,0,1] neg_hi:[0,0,1]
	v_add_f32_e32 v36, v70, v36
	v_pk_mul_f32 v[50:51], v[50:51], v[98:99] op_sel_hi:[1,0]
	v_pk_mul_f32 v[48:49], v[44:45], v[44:45]
	v_add_f32_e32 v36, v71, v36
	v_pk_fma_f32 v[46:47], v[46:47], v[96:97], v[50:51] op_sel_hi:[1,0,1] neg_lo:[0,0,1] neg_hi:[0,0,1]
	v_add_f32_e32 v36, v48, v36
	v_pk_mul_f32 v[72:73], v[72:73], v[98:99] op_sel_hi:[1,0]
	v_pk_mul_f32 v[50:51], v[46:47], v[46:47]
	v_add_f32_e32 v36, v49, v36
	v_pk_fma_f32 v[52:53], v[52:53], v[96:97], v[72:73] op_sel_hi:[1,0,1] neg_lo:[0,0,1] neg_hi:[0,0,1]
	v_add_f32_e32 v36, v50, v36
	v_pk_mul_f32 v[74:75], v[74:75], v[98:99] op_sel_hi:[1,0]
	v_pk_mul_f32 v[72:73], v[52:53], v[52:53]
	v_add_f32_e32 v36, v51, v36
	v_pk_fma_f32 v[54:55], v[54:55], v[96:97], v[74:75] op_sel_hi:[1,0,1] neg_lo:[0,0,1] neg_hi:[0,0,1]
	v_add_f32_e32 v36, v72, v36
	v_pk_mul_f32 v[84:85], v[84:85], v[98:99] op_sel_hi:[1,0]
	v_pk_mul_f32 v[74:75], v[54:55], v[54:55]
	v_add_f32_e32 v36, v73, v36
	v_pk_fma_f32 v[76:77], v[76:77], v[96:97], v[84:85] op_sel_hi:[1,0,1] neg_lo:[0,0,1] neg_hi:[0,0,1]
	v_add_f32_e32 v36, v74, v36
	v_pk_mul_f32 v[86:87], v[86:87], v[98:99] op_sel_hi:[1,0]
	v_pk_mul_f32 v[84:85], v[76:77], v[76:77]
	v_add_f32_e32 v36, v75, v36
	v_pk_fma_f32 v[78:79], v[78:79], v[96:97], v[86:87] op_sel_hi:[1,0,1] neg_lo:[0,0,1] neg_hi:[0,0,1]
	v_add_f32_e32 v36, v84, v36
	v_pk_mul_f32 v[92:93], v[92:93], v[98:99] op_sel_hi:[1,0]
	v_pk_mul_f32 v[86:87], v[78:79], v[78:79]
	v_add_f32_e32 v36, v85, v36
	v_pk_fma_f32 v[88:89], v[88:89], v[96:97], v[92:93] op_sel_hi:[1,0,1] neg_lo:[0,0,1] neg_hi:[0,0,1]
	v_add_f32_e32 v36, v86, v36
	v_pk_mul_f32 v[94:95], v[94:95], v[98:99] op_sel_hi:[1,0]
	v_pk_mul_f32 v[92:93], v[88:89], v[88:89]
	v_add_f32_e32 v36, v87, v36
	v_pk_fma_f32 v[90:91], v[90:91], v[96:97], v[94:95] op_sel_hi:[1,0,1] neg_lo:[0,0,1] neg_hi:[0,0,1]
	v_add_f32_e32 v36, v92, v36
	v_pk_mul_f32 v[94:95], v[90:91], v[90:91]
	v_add_f32_e32 v36, v93, v36
	v_add_f32_e32 v36, v94, v36
	v_add_f32_e32 v36, v95, v36
	ds_swizzle_b32 v37, v36 offset:swizzle(SWAP,16)
	v_readlane_b32 s73, v254, 42
	v_readlane_b32 s74, v254, 43
	v_readlane_b32 s75, v254, 44
	v_readlane_b32 s76, v254, 45
	s_waitcnt lgkmcnt(0)
; DI unsigned pk2(float lo, float hi) { const f32x2 v = {lo, hi}; return __builtin_bit_cast(unsigned, __builtin_convertvector(v, bf16x2_t)); }
; DI void attn_block(const Params& P, const Frame& F, int L, int b, int h, int qb, float lam, float oml) {
;     ...
;     const float r = oml * __builtin_amdgcn_rsqf(ss * (1.0f / 128.0f) + EPS);
;     unsigned long long ov[8];
; #pragma unroll
;     for (int d = 0; d < 8; ++d) ov[d] = (unsigned long long)pk2(O[0][d][0] * r * nwv[d][0], O[0][d][1] * r * nwv[d][1]) | ((unsigned long long)pk2(O[0][d][2] * r * nwv[d][2], O[0][d][3] * r * nwv[d][3]) << 32);
; #pragma unroll
;     for (int d = 0; d < 8; ++d) *(unsigned long long*)(MIX + (rowbase + qrow) * D + 512 + h * 128 + 16 * d + 4 * rq) = ov[d];
	v_add_f32_e32 v36, v36, v37
	ds_bpermute_b32 v37, v190, v36
	v_readlane_b32 s77, v254, 46
	v_readlane_b32 s78, v254, 47
	v_readlane_b32 s79, v254, 48
	v_readlane_b32 s80, v254, 49
	s_waitcnt lgkmcnt(0)
	v_add_f32_e32 v36, v36, v37
	v_fmamk_f32 v36, v36, 0x3c000000, v179
	v_rsq_f32_e32 v36, v36
	v_readlane_b32 s81, v254, 50
	v_readlane_b32 s82, v254, 51
	v_readlane_b32 s83, v254, 52
	v_mul_f32_e32 v36, 0x3f4ccccd, v36
	v_pk_mul_f32 v[32:33], v[32:33], v[36:37] op_sel_hi:[1,0]
	v_readlane_b32 s69, v254, 38
	s_waitcnt vmcnt(7)
	v_pk_mul_f32 v[0:1], v[0:1], v[32:33]
	v_pk_mul_f32 v[32:33], v[34:35], v[36:37] op_sel_hi:[1,0]
	v_cvt_pk_bf16_f32 v0, v0, v1
	v_pk_mul_f32 v[2:3], v[2:3], v[32:33]
	s_nop 0
	v_cvt_pk_bf16_f32 v1, v2, v3
	v_pk_mul_f32 v[2:3], v[40:41], v[36:37] op_sel_hi:[1,0]
	s_waitcnt vmcnt(6)
	v_pk_mul_f32 v[2:3], v[4:5], v[2:3]
	v_pk_mul_f32 v[4:5], v[42:43], v[36:37] op_sel_hi:[1,0]
	v_cvt_pk_bf16_f32 v2, v2, v3
	v_pk_mul_f32 v[4:5], v[6:7], v[4:5]
	v_pk_mul_f32 v[6:7], v[62:63], v[36:37] op_sel_hi:[1,0]
	v_cvt_pk_bf16_f32 v3, v4, v5
	v_pk_mul_f32 v[4:5], v[60:61], v[36:37] op_sel_hi:[1,0]
	s_waitcnt vmcnt(5)
	v_pk_mul_f32 v[6:7], v[10:11], v[6:7]
	v_pk_mul_f32 v[4:5], v[8:9], v[4:5]
	v_pk_mul_f32 v[8:9], v[66:67], v[36:37] op_sel_hi:[1,0]
	v_cvt_pk_bf16_f32 v4, v4, v5
	v_cvt_pk_bf16_f32 v5, v6, v7
	v_pk_mul_f32 v[6:7], v[64:65], v[36:37] op_sel_hi:[1,0]
	s_waitcnt vmcnt(4)
	v_pk_mul_f32 v[8:9], v[14:15], v[8:9]
	v_pk_mul_f32 v[6:7], v[12:13], v[6:7]
	v_pk_mul_f32 v[10:11], v[46:47], v[36:37] op_sel_hi:[1,0]
	v_cvt_pk_bf16_f32 v6, v6, v7
	v_cvt_pk_bf16_f32 v7, v8, v9
	v_pk_mul_f32 v[8:9], v[44:45], v[36:37] op_sel_hi:[1,0]
	s_waitcnt vmcnt(3)
	v_pk_mul_f32 v[10:11], v[18:19], v[10:11]
	v_pk_mul_f32 v[8:9], v[16:17], v[8:9]
	v_pk_mul_f32 v[12:13], v[54:55], v[36:37] op_sel_hi:[1,0]
	v_cvt_pk_bf16_f32 v8, v8, v9
	v_cvt_pk_bf16_f32 v9, v10, v11
	v_pk_mul_f32 v[10:11], v[52:53], v[36:37] op_sel_hi:[1,0]
	s_waitcnt vmcnt(2)
	v_pk_mul_f32 v[12:13], v[22:23], v[12:13]
	v_pk_mul_f32 v[10:11], v[20:21], v[10:11]
	v_pk_mul_f32 v[14:15], v[78:79], v[36:37] op_sel_hi:[1,0]
	v_cvt_pk_bf16_f32 v10, v10, v11
	v_cvt_pk_bf16_f32 v11, v12, v13
	v_pk_mul_f32 v[12:13], v[76:77], v[36:37] op_sel_hi:[1,0]
	s_waitcnt vmcnt(1)
	v_pk_mul_f32 v[14:15], v[26:27], v[14:15]
	v_pk_mul_f32 v[12:13], v[24:25], v[12:13]
	v_pk_mul_f32 v[16:17], v[90:91], v[36:37] op_sel_hi:[1,0]
	v_cvt_pk_bf16_f32 v12, v12, v13
	v_cvt_pk_bf16_f32 v13, v14, v15
	v_pk_mul_f32 v[14:15], v[88:89], v[36:37] op_sel_hi:[1,0]
	s_waitcnt vmcnt(0)
	v_pk_mul_f32 v[16:17], v[30:31], v[16:17]
	v_pk_mul_f32 v[14:15], v[28:29], v[14:15]
	s_nop 0
	v_cvt_pk_bf16_f32 v14, v14, v15
	v_cvt_pk_bf16_f32 v15, v16, v17
	v_lshlrev_b64 v[16:17], 12, v[142:143]
	v_lshl_add_u64 v[16:17], s[54:55], 0, v[16:17]
	v_lshl_add_u64 v[16:17], v[16:17], 0, s[38:39]
	v_lshl_add_u64 v[16:17], v[130:131], 1, v[16:17]
	v_lshl_add_u64 v[18:19], v[16:17], 0, s[6:7]
	s_mov_b32 s6, 0x61400000
	v_add_co_u32_e32 v16, vcc, s6, v16
	s_mov_b64 s[6:7], 0
	s_nop 0
	v_addc_co_u32_e32 v17, vcc, 0, v17, vcc
	global_store_dwordx2 v[16:17], v[0:1], off offset:1024
	global_store_dwordx2 v[18:19], v[2:3], off offset:32
	global_store_dwordx2 v[18:19], v[4:5], off offset:64
	global_store_dwordx2 v[18:19], v[6:7], off offset:96
	global_store_dwordx2 v[18:19], v[8:9], off offset:128
	global_store_dwordx2 v[18:19], v[10:11], off offset:160
	global_store_dwordx2 v[18:19], v[12:13], off offset:192
	global_store_dwordx2 v[18:19], v[14:15], off offset:224

; template <int L> DI void layer_phases(const Params& P, Frame& F, const XcdBarrier& bar, int lo, int hi) {
;     ...
;             for (;;) {
;                 __syncthreads();
;                 if (F.tid == 0) F.MISC[24] = __hip_atomic_fetch_add(qctr, 1u, __ATOMIC_RELAXED, __HIP_MEMORY_SCOPE_AGENT);
;                 __syncthreads();
;                 const int u = (int)F.MISC[24];
.LBB0_1048:
	s_barrier
	s_and_saveexec_b64 s[6:7], s[4:5]
	s_cbranch_execz .LBB0_1052
	s_waitcnt vmcnt(0)
	v_mov_b32_e32 v1, s65
	ds_write_b32 v1, v252

.LBB0_1115:
	s_cmp_lt_u32 s3, 0x40001
	s_mov_b64 s[18:19], 0
	s_cselect_b64 s[20:21], -1, 0
	s_mov_b64 s[22:23], -1
	s_and_b64 vcc, exec, s[20:21]
	s_cbranch_vccnz .LBB0_1112
	s_branch .LBB0_1109
	s_nop 0
	s_nop 0
	s_nop 0
	s_nop 0
.LBB0_1116:
	s_or_b64 exec, exec, s[14:15]
	s_and_b64 s[14:15], s[16:17], exec

; DI float wave_sum(float v) { v += shx<1>(v); v += shx<2>(v); v += shx<4>(v); v += shx<8>(v); v += shx<16>(v); v += shx<32>(v); return v; }
; template <int L> DI void layer_phases(const Params& P, Frame& F, const XcdBarrier& bar, int lo, int hi) {
;     ...
;             const float li = (L == 0) ? 0.2f : 0.35550906759f;
;             const float d1 = wave_sum(P.in[I_LQ1][L * 64 + F.lane] * P.in[I_LK1][L * 64 + F.lane]), d2 = wave_sum(P.in[I_LQ2][L * 64 + F.lane] * P.in[I_LK2][L * 64 + F.lane]);
;             const float lam = __expf(d1) - __expf(d2) + li;
;             unsigned* qctr = (unsigned*)(ws + WS_CTL) + CW_QUEUE + 64 * L;
;             for (;;) {
;                 __syncthreads();
;                 if (F.tid == 0) F.MISC[24] = __hip_atomic_fetch_add(qctr, 1u, __ATOMIC_RELAXED, __HIP_MEMORY_SCOPE_AGENT);
.LBB0_2610:
	v_ashrrev_i32_e32 v113, 31, v112
	v_readlane_b32 s4, v254, 5
	v_lshlrev_b64 v[0:1], 2, v[112:113]
	v_readlane_b32 s6, v254, 7
	v_readlane_b32 s7, v254, 8
	v_readlane_b32 s8, v254, 9
	v_readlane_b32 s9, v254, 10
	v_lshl_add_u64 v[2:3], s[6:7], 0, v[0:1]
	v_readlane_b32 s10, v254, 11
	v_readlane_b32 s11, v254, 12
	v_readlane_b32 s12, v254, 13
	v_readlane_b32 s13, v254, 14
	global_load_dword v4, v[2:3], off offset:256
	v_lshl_add_u64 v[2:3], s[8:9], 0, v[0:1]
	global_load_dword v5, v[2:3], off offset:256
	v_lshl_add_u64 v[2:3], s[10:11], 0, v[0:1]
	v_lshl_add_u64 v[0:1], s[12:13], 0, v[0:1]
	global_load_dword v2, v[2:3], off offset:256
	v_xor_b32_e32 v3, 32, v154
	global_load_dword v1, v[0:1], off offset:256
	v_and_b32_e32 v0, 64, v154
	v_add_u32_e32 v12, 64, v0
	v_ashrrev_i32_e32 v6, 4, v112
	v_cmp_lt_i32_e32 vcc, v3, v12
	v_add_u32_e32 v8, 0x200, v114
	v_bfe_u32 v9, v112, 3, 1
	s_movk_i32 s6, 0x2400
	v_bfe_u32 v11, v112, 2, 2
	v_lshlrev_b32_e32 v106, 2, v6
	v_cndmask_b32_e32 v3, v154, v3, vcc
	v_ashrrev_i32_e32 v104, 4, v8
	v_mul_u32_u24_e32 v182, 0x2400, v9
	v_mad_u32_u24 v8, v9, s6, 0
	v_or_b32_e32 v9, v106, v11
	v_lshlrev_b32_e32 v190, 2, v3
	v_lshlrev_b32_e32 v7, 3, v112
	v_ashrrev_i32_e32 v98, 4, v114
	s_movk_i32 s7, 0x90
	s_movk_i32 s8, 0x110
	v_and_b32_e32 v0, 24, v7
	v_mul_lo_u32 v183, v98, s7
	v_mul_lo_u32 v188, v104, s7
	s_add_u32 s0, s54, 0x2100
	s_addc_u32 s1, s55, 0
	v_lshlrev_b32_e32 v10, 4, v112
	s_add_u32 s56, s54, 0x41600000
	v_and_b32_e32 v103, 15, v112
	v_lshlrev_b32_e32 v100, 3, v6
	v_and_b32_e32 v184, 0x70, v10
	v_add_u32_e32 v6, v8, v183
	s_addc_u32 s57, s55, 0
	s_lshl_b32 s66, s86, 4
	v_mul_lo_u32 v185, v98, s8
	v_mul_lo_u32 v189, v104, s8
	v_sub_u32_e32 v10, v106, v103
	v_readlane_b32 s5, v254, 6
	v_readlane_b32 s14, v254, 15
	v_readlane_b32 s15, v254, 16
	v_and_b32_e32 v102, 0x78, v7
	v_lshlrev_b32_e32 v186, 4, v103
	v_add_u32_e32 v7, 0, v185
	v_ashrrev_i32_e32 v107, 31, v106
	s_mov_b32 s41, 0
	v_cmp_eq_u32_e64 s[4:5], 0, v114
	v_mov_b32_e32 v97, 0
	v_and_b32_e32 v145, -16, v112
	s_movk_i32 s3, 0x3ff
	s_movk_i32 s33, 0x3800
	s_mov_b64 s[42:43], 0x1800
	s_movk_i32 s47, 0x1000
	s_mov_b32 s62, 0x42fc0000
	s_mov_b32 s46, 0x3e38aa3b
	s_movk_i32 s63, 0x2000
	s_mov_b32 s64, 0xff800000
	v_mov_b32_e32 v163, 0x358637bd
	s_mov_b64 s[48:49], 0x61400400
	s_mov_b32 s65, 0x61400000
	v_mov_b32_e32 v180, 0x42800000
	v_mov_b32_e32 v181, 0x3fb8aa3b
	v_ashrrev_i32_e32 v99, 31, v98
	v_mul_u32_u24_e32 v187, 0x90, v103
	v_ashrrev_i32_e32 v101, 31, v100
	v_ashrrev_i32_e32 v105, 31, v104
	v_lshl_add_u64 v[110:111], v[106:107], 2, s[14:15]
	s_add_i32 s67, 0, 0x22060
	v_add_u32_e32 v191, v7, v186
	v_mov_b32_e32 v112, 2.0
	v_mov_b32_e32 v113, 0x40400000
	v_mov_b32_e32 v114, 0x41800000
	v_mov_b32_e32 v115, 0x41880000
	v_mov_b32_e32 v116, 0x41900000
	v_mov_b32_e32 v117, 0x41980000
	v_mov_b32_e32 v118, 0x42000000
	v_mov_b32_e32 v119, 0x42040000
	s_waitcnt vmcnt(2)
	v_mul_f32_e32 v3, v4, v5
	v_mov_b32_e32 v120, 0x42080000
	v_mov_b32_e32 v121, 0x420c0000
	v_mov_b32_dpp v3, v3 quad_perm:[1,0,3,2] row_mask:0xf bank_mask:0xf bound_ctrl:1
	v_fmac_f32_e32 v3, v4, v5
	s_waitcnt vmcnt(0)
	v_mul_f32_e32 v11, v2, v1
	v_add_u32_e32 v5, v8, v188
	v_add_u32_e32 v8, 0, v189
	v_mov_b32_dpp v11, v11 quad_perm:[1,0,3,2] row_mask:0xf bank_mask:0xf bound_ctrl:1
	v_fmac_f32_e32 v11, v2, v1
	v_add_f32_dpp v1, v3, v3 quad_perm:[2,3,0,1] row_mask:0xf bank_mask:0xf bound_ctrl:1
	ds_swizzle_b32 v3, v1 offset:swizzle(SWAP,4)
	v_add_f32_dpp v2, v11, v11 quad_perm:[2,3,0,1] row_mask:0xf bank_mask:0xf bound_ctrl:1
	ds_swizzle_b32 v4, v2 offset:swizzle(SWAP,4)
	v_add_u32_e32 v193, v5, v184
	v_add_u32_e32 v194, v8, v186
	s_waitcnt lgkmcnt(1)
	v_add_f32_e32 v1, v1, v3
	ds_swizzle_b32 v3, v1 offset:swizzle(SWAP,8)
	s_waitcnt lgkmcnt(1)
	v_add_f32_e32 v2, v2, v4
	ds_swizzle_b32 v4, v2 offset:swizzle(SWAP,8)
	v_mad_u64_u32 v[108:109], s[6:7], v9, s8, v[0:1]
	s_waitcnt lgkmcnt(1)
	v_add_f32_e32 v0, v1, v3
	v_add_u32_e32 v109, v6, v184
	s_waitcnt lgkmcnt(0)
	v_add_f32_e32 v1, v2, v4
	ds_swizzle_b32 v2, v0 offset:swizzle(SWAP,16)
	ds_swizzle_b32 v3, v1 offset:swizzle(SWAP,16)
	v_or_b32_e32 v6, s66, v103
	v_subrev_u32_e32 v4, s66, v10
	v_add_u32_e32 v195, 64, v4
	s_waitcnt lgkmcnt(1)
	v_add_f32_e32 v0, v0, v2
	s_waitcnt lgkmcnt(0)
	v_add_f32_e32 v1, v1, v3
	ds_bpermute_b32 v2, v190, v0
	ds_bpermute_b32 v3, v190, v1
	v_mov_b32_e32 v122, 0x42400000
	v_mov_b32_e32 v123, 0x42440000
	v_mov_b32_e32 v124, 0x42480000
	s_waitcnt lgkmcnt(1)
	v_add_f32_e32 v0, v0, v2
	s_waitcnt lgkmcnt(0)
	v_add_f32_e32 v1, v1, v3
	v_mul_f32_e32 v0, 0x3fb8aa3b, v0
	v_mul_f32_e32 v1, 0x3fb8aa3b, v1
	v_exp_f32_e32 v0, v0
	v_exp_f32_e32 v1, v1
	v_sub_u32_e32 v2, v6, v106
	v_subrev_u32_e32 v196, 64, v2
	v_mov_b32_e32 v125, 0x424c0000
	v_sub_f32_e32 v0, v0, v1
	v_add_f32_e32 v197, 0x3eb60549, v0
	v_mov_b32_e32 v198, 0xff800000
	v_readlane_b32 s16, v254, 17
	v_readlane_b32 s17, v254, 18
	v_readlane_b32 s18, v254, 19
	v_readlane_b32 s19, v254, 20
	s_mov_b64 s[6:7], exec
	s_and_b64 exec, exec, s[4:5]
	v_mov_b32_e32 v252, 1
	global_atomic_add v252, v97, v252, s[0:1] sc0
	s_mov_b64 exec, s[6:7]
	s_branch .LBB0_2613
; DI void attn_block(const Params& P, const Frame& F, int L, int b, int h, int qb, float lam, float oml) {
;     ...
;     const float* nw = P.in[I_DIFF_NORM] + L * 128;
;     f32x4 nwv[8];
; #pragma unroll
;     for (int d = 0; d < 8; ++d) nwv[d] = *(const f32x4*)(nw + 16 * d + 4 * rq);
;     float inv[2];
; #pragma unroll
;     for (int j = 0; j < 2; ++j) { float l = lrun[j]; l += shx<16>(l); l += shx<32>(l); inv[j] = __builtin_amdgcn_rcpf(l); }
;     const float inv1l = lam * inv[1];
;     float ss = 0.f;
; #pragma unroll
;     for (int d = 0; d < 8; ++d)
; #pragma unroll
;         for (int e = 0; e < 4; ++e) { const float o = O[0][d][e] * inv[0] - O[1][d][e] * inv1l; O[0][d][e] = o; ss += o * o; }
;     ss += shx<16>(ss); ss += shx<32>(ss);
.LBB0_2611:
	global_load_dwordx4 v[0:3], v[110:111], off offset:512
	global_load_dwordx4 v[4:7], v[110:111], off offset:576
	ds_swizzle_b32 v8, v202 offset:swizzle(SWAP,16)
	ds_swizzle_b32 v9, v203 offset:swizzle(SWAP,16)
	s_lshl_b32 s40, s68, 1
	v_readlane_b32 s68, v254, 37
	s_mov_b64 s[6:7], 0
	s_waitcnt vmcnt(2) lgkmcnt(1)
	s_mov_b64 s[6:7], exec
	s_and_b64 exec, exec, s[4:5]
	v_mov_b32_e32 v252, 1
	global_atomic_add v252, v97, v252, s[0:1] sc0
	s_mov_b64 exec, s[6:7]
	s_mov_b64 s[6:7], 0
	v_add_f32_e32 v24, v202, v8
	s_waitcnt lgkmcnt(0)
	v_add_f32_e32 v25, v203, v9
	ds_bpermute_b32 v26, v190, v24
	ds_bpermute_b32 v27, v190, v25
	global_load_dwordx4 v[8:11], v[110:111], off offset:640
	global_load_dwordx4 v[12:15], v[110:111], off offset:704
	global_load_dwordx4 v[16:19], v[110:111], off offset:768
	global_load_dwordx4 v[20:23], v[110:111], off offset:832
	v_readlane_b32 s70, v254, 39
	v_readlane_b32 s71, v254, 40
	s_waitcnt lgkmcnt(1)
	v_add_f32_e32 v24, v24, v26
	s_waitcnt lgkmcnt(0)
	v_add_f32_e32 v25, v25, v27
	v_rcp_f32_e32 v128, v25
	v_rcp_f32_e32 v96, v24
	global_load_dwordx4 v[24:27], v[110:111], off offset:896
	global_load_dwordx4 v[28:31], v[110:111], off offset:960
	v_readlane_b32 s69, v254, 38
	v_mul_f32_e32 v128, v197, v128
	v_pk_mul_f32 v[36:37], v[36:37], v[128:129] op_sel_hi:[1,0]
	v_pk_mul_f32 v[38:39], v[38:39], v[128:129] op_sel_hi:[1,0]
	v_pk_fma_f32 v[32:33], v[32:33], v[96:97], v[36:37] op_sel_hi:[1,0,1] neg_lo:[0,0,1] neg_hi:[0,0,1]
	v_pk_fma_f32 v[34:35], v[34:35], v[96:97], v[38:39] op_sel_hi:[1,0,1] neg_lo:[0,0,1] neg_hi:[0,0,1]
	v_pk_mul_f32 v[36:37], v[32:33], v[32:33]
	v_pk_mul_f32 v[44:45], v[44:45], v[128:129] op_sel_hi:[1,0]
	v_pk_mul_f32 v[38:39], v[34:35], v[34:35]
	v_add_f32_e32 v36, v36, v37
	v_pk_fma_f32 v[40:41], v[40:41], v[96:97], v[44:45] op_sel_hi:[1,0,1] neg_lo:[0,0,1] neg_hi:[0,0,1]
	v_add_f32_e32 v36, v38, v36
	v_pk_mul_f32 v[46:47], v[46:47], v[128:129] op_sel_hi:[1,0]
	v_pk_mul_f32 v[44:45], v[40:41], v[40:41]
	v_add_f32_e32 v36, v39, v36
	v_pk_fma_f32 v[42:43], v[42:43], v[96:97], v[46:47] op_sel_hi:[1,0,1] neg_lo:[0,0,1] neg_hi:[0,0,1]
	v_add_f32_e32 v36, v44, v36
	v_pk_mul_f32 v[56:57], v[56:57], v[128:129] op_sel_hi:[1,0]
	v_pk_mul_f32 v[46:47], v[42:43], v[42:43]
	v_add_f32_e32 v36, v45, v36
	v_pk_fma_f32 v[48:49], v[48:49], v[96:97], v[56:57] op_sel_hi:[1,0,1] neg_lo:[0,0,1] neg_hi:[0,0,1]
	v_add_f32_e32 v36, v46, v36
	v_pk_mul_f32 v[58:59], v[58:59], v[128:129] op_sel_hi:[1,0]
	v_pk_mul_f32 v[56:57], v[48:49], v[48:49]
	v_add_f32_e32 v36, v47, v36
	v_pk_fma_f32 v[50:51], v[50:51], v[96:97], v[58:59] op_sel_hi:[1,0,1] neg_lo:[0,0,1] neg_hi:[0,0,1]
	v_add_f32_e32 v36, v56, v36
	v_pk_mul_f32 v[64:65], v[64:65], v[128:129] op_sel_hi:[1,0]
	v_pk_mul_f32 v[58:59], v[50:51], v[50:51]
	v_add_f32_e32 v36, v57, v36
	v_pk_fma_f32 v[52:53], v[52:53], v[96:97], v[64:65] op_sel_hi:[1,0,1] neg_lo:[0,0,1] neg_hi:[0,0,1]
	v_add_f32_e32 v36, v58, v36
	v_pk_mul_f32 v[66:67], v[66:67], v[128:129] op_sel_hi:[1,0]
	v_pk_mul_f32 v[64:65], v[52:53], v[52:53]
	v_add_f32_e32 v36, v59, v36
	v_pk_fma_f32 v[54:55], v[54:55], v[96:97], v[66:67] op_sel_hi:[1,0,1] neg_lo:[0,0,1] neg_hi:[0,0,1]
	v_add_f32_e32 v36, v64, v36
	v_pk_mul_f32 v[68:69], v[68:69], v[128:129] op_sel_hi:[1,0]
	v_pk_mul_f32 v[66:67], v[54:55], v[54:55]
	v_add_f32_e32 v36, v65, v36
	v_pk_fma_f32 v[60:61], v[60:61], v[96:97], v[68:69] op_sel_hi:[1,0,1] neg_lo:[0,0,1] neg_hi:[0,0,1]
	v_add_f32_e32 v36, v66, v36
	v_pk_mul_f32 v[70:71], v[70:71], v[128:129] op_sel_hi:[1,0]
	v_pk_mul_f32 v[68:69], v[60:61], v[60:61]
	v_add_f32_e32 v36, v67, v36
	v_pk_fma_f32 v[62:63], v[62:63], v[96:97], v[70:71] op_sel_hi:[1,0,1] neg_lo:[0,0,1] neg_hi:[0,0,1]
	v_add_f32_e32 v36, v68, v36
	v_pk_mul_f32 v[76:77], v[76:77], v[128:129] op_sel_hi:[1,0]
	v_pk_mul_f32 v[70:71], v[62:63], v[62:63]
	v_add_f32_e32 v36, v69, v36
	v_pk_fma_f32 v[72:73], v[72:73], v[96:97], v[76:77] op_sel_hi:[1,0,1] neg_lo:[0,0,1] neg_hi:[0,0,1]
	v_add_f32_e32 v36, v70, v36
	v_pk_mul_f32 v[78:79], v[78:79], v[128:129] op_sel_hi:[1,0]
	v_pk_mul_f32 v[76:77], v[72:73], v[72:73]
	v_add_f32_e32 v36, v71, v36
	v_pk_fma_f32 v[74:75], v[74:75], v[96:97], v[78:79] op_sel_hi:[1,0,1] neg_lo:[0,0,1] neg_hi:[0,0,1]
	v_add_f32_e32 v36, v76, v36
	v_pk_mul_f32 v[84:85], v[84:85], v[128:129] op_sel_hi:[1,0]
	v_pk_mul_f32 v[78:79], v[74:75], v[74:75]
	v_add_f32_e32 v36, v77, v36
	v_pk_fma_f32 v[80:81], v[80:81], v[96:97], v[84:85] op_sel_hi:[1,0,1] neg_lo:[0,0,1] neg_hi:[0,0,1]
	v_add_f32_e32 v36, v78, v36
	v_pk_mul_f32 v[86:87], v[86:87], v[128:129] op_sel_hi:[1,0]
	v_pk_mul_f32 v[84:85], v[80:81], v[80:81]
	v_add_f32_e32 v36, v79, v36
	v_pk_fma_f32 v[82:83], v[82:83], v[96:97], v[86:87] op_sel_hi:[1,0,1] neg_lo:[0,0,1] neg_hi:[0,0,1]
	v_add_f32_e32 v36, v84, v36
	v_pk_mul_f32 v[92:93], v[92:93], v[128:129] op_sel_hi:[1,0]
	v_pk_mul_f32 v[86:87], v[82:83], v[82:83]
	v_add_f32_e32 v36, v85, v36
	v_pk_fma_f32 v[88:89], v[88:89], v[96:97], v[92:93] op_sel_hi:[1,0,1] neg_lo:[0,0,1] neg_hi:[0,0,1]
	v_add_f32_e32 v36, v86, v36
	v_pk_mul_f32 v[94:95], v[94:95], v[128:129] op_sel_hi:[1,0]
	v_pk_mul_f32 v[92:93], v[88:89], v[88:89]
	v_add_f32_e32 v36, v87, v36
	v_pk_fma_f32 v[90:91], v[90:91], v[96:97], v[94:95] op_sel_hi:[1,0,1] neg_lo:[0,0,1] neg_hi:[0,0,1]
	v_add_f32_e32 v36, v92, v36
	v_pk_mul_f32 v[94:95], v[90:91], v[90:91]
	v_add_f32_e32 v36, v93, v36
	v_add_f32_e32 v36, v94, v36
	v_add_f32_e32 v36, v95, v36
	ds_swizzle_b32 v37, v36 offset:swizzle(SWAP,16)
	v_readlane_b32 s72, v254, 41
	v_readlane_b32 s73, v254, 42
	v_readlane_b32 s74, v254, 43
	v_readlane_b32 s75, v254, 44
	s_waitcnt lgkmcnt(0)
; DI unsigned pk2(float lo, float hi) { const f32x2 v = {lo, hi}; return __builtin_bit_cast(unsigned, __builtin_convertvector(v, bf16x2_t)); }
; DI void attn_block(const Params& P, const Frame& F, int L, int b, int h, int qb, float lam, float oml) {
;     ...
;     const float r = oml * __builtin_amdgcn_rsqf(ss * (1.0f / 128.0f) + EPS);
;     unsigned long long ov[8];
; #pragma unroll
;     for (int d = 0; d < 8; ++d) ov[d] = (unsigned long long)pk2(O[0][d][0] * r * nwv[d][0], O[0][d][1] * r * nwv[d][1]) | ((unsigned long long)pk2(O[0][d][2] * r * nwv[d][2], O[0][d][3] * r * nwv[d][3]) << 32);
; #pragma unroll
;     for (int d = 0; d < 8; ++d) *(unsigned long long*)(MIX + (rowbase + qrow) * D + 512 + h * 128 + 16 * d + 4 * rq) = ov[d];
	v_add_f32_e32 v36, v36, v37
	ds_bpermute_b32 v37, v190, v36
	v_readlane_b32 s76, v254, 45
	v_readlane_b32 s77, v254, 46
	v_readlane_b32 s78, v254, 47
	v_readlane_b32 s79, v254, 48
	s_waitcnt lgkmcnt(0)
	v_add_f32_e32 v36, v36, v37
	v_fmamk_f32 v36, v36, 0x3c000000, v163
	v_rsq_f32_e32 v36, v36
	v_readlane_b32 s80, v254, 49
	v_readlane_b32 s81, v254, 50
	v_readlane_b32 s82, v254, 51
	v_mul_f32_e32 v36, 0x3f24fd5c, v36
	v_pk_mul_f32 v[32:33], v[32:33], v[36:37] op_sel_hi:[1,0]
	v_readlane_b32 s83, v254, 52
	s_waitcnt vmcnt(7)
	v_pk_mul_f32 v[0:1], v[0:1], v[32:33]
	v_pk_mul_f32 v[32:33], v[34:35], v[36:37] op_sel_hi:[1,0]
	v_cvt_pk_bf16_f32 v0, v0, v1
	v_pk_mul_f32 v[2:3], v[2:3], v[32:33]
	s_nop 0
	v_cvt_pk_bf16_f32 v1, v2, v3
	v_pk_mul_f32 v[2:3], v[40:41], v[36:37] op_sel_hi:[1,0]
	s_waitcnt vmcnt(6)
	v_pk_mul_f32 v[2:3], v[4:5], v[2:3]
	v_pk_mul_f32 v[4:5], v[42:43], v[36:37] op_sel_hi:[1,0]
	v_cvt_pk_bf16_f32 v2, v2, v3
	v_pk_mul_f32 v[4:5], v[6:7], v[4:5]
	v_pk_mul_f32 v[6:7], v[50:51], v[36:37] op_sel_hi:[1,0]
	v_cvt_pk_bf16_f32 v3, v4, v5
	v_pk_mul_f32 v[4:5], v[48:49], v[36:37] op_sel_hi:[1,0]
	s_waitcnt vmcnt(5)
	v_pk_mul_f32 v[6:7], v[10:11], v[6:7]
	v_pk_mul_f32 v[4:5], v[8:9], v[4:5]
	v_pk_mul_f32 v[8:9], v[54:55], v[36:37] op_sel_hi:[1,0]
	v_cvt_pk_bf16_f32 v4, v4, v5
	v_cvt_pk_bf16_f32 v5, v6, v7
	v_pk_mul_f32 v[6:7], v[52:53], v[36:37] op_sel_hi:[1,0]
	s_waitcnt vmcnt(4)
	v_pk_mul_f32 v[8:9], v[14:15], v[8:9]
	v_pk_mul_f32 v[6:7], v[12:13], v[6:7]
	v_pk_mul_f32 v[10:11], v[62:63], v[36:37] op_sel_hi:[1,0]
	v_cvt_pk_bf16_f32 v6, v6, v7
	v_cvt_pk_bf16_f32 v7, v8, v9
	v_pk_mul_f32 v[8:9], v[60:61], v[36:37] op_sel_hi:[1,0]
	s_waitcnt vmcnt(3)
	v_pk_mul_f32 v[10:11], v[18:19], v[10:11]
	v_pk_mul_f32 v[8:9], v[16:17], v[8:9]
	v_pk_mul_f32 v[12:13], v[74:75], v[36:37] op_sel_hi:[1,0]
	v_cvt_pk_bf16_f32 v8, v8, v9
	v_cvt_pk_bf16_f32 v9, v10, v11
	v_pk_mul_f32 v[10:11], v[72:73], v[36:37] op_sel_hi:[1,0]
	s_waitcnt vmcnt(2)
	v_pk_mul_f32 v[12:13], v[22:23], v[12:13]
	v_pk_mul_f32 v[10:11], v[20:21], v[10:11]
	v_pk_mul_f32 v[14:15], v[82:83], v[36:37] op_sel_hi:[1,0]
	v_cvt_pk_bf16_f32 v10, v10, v11
	v_cvt_pk_bf16_f32 v11, v12, v13
	v_pk_mul_f32 v[12:13], v[80:81], v[36:37] op_sel_hi:[1,0]
	s_waitcnt vmcnt(1)
	v_pk_mul_f32 v[14:15], v[26:27], v[14:15]
	v_pk_mul_f32 v[12:13], v[24:25], v[12:13]
	v_pk_mul_f32 v[16:17], v[90:91], v[36:37] op_sel_hi:[1,0]
	v_cvt_pk_bf16_f32 v12, v12, v13
	v_cvt_pk_bf16_f32 v13, v14, v15
	v_pk_mul_f32 v[14:15], v[88:89], v[36:37] op_sel_hi:[1,0]
	s_waitcnt vmcnt(0)
	v_pk_mul_f32 v[16:17], v[30:31], v[16:17]
	v_pk_mul_f32 v[14:15], v[28:29], v[14:15]
	s_nop 0
	v_cvt_pk_bf16_f32 v14, v14, v15
	v_cvt_pk_bf16_f32 v15, v16, v17
	v_lshlrev_b64 v[16:17], 12, v[126:127]
	v_lshl_add_u64 v[16:17], s[54:55], 0, v[16:17]
	v_lshl_add_u64 v[16:17], v[16:17], 0, s[40:41]
	v_lshl_add_u64 v[16:17], v[106:107], 1, v[16:17]
	v_lshl_add_u64 v[18:19], v[16:17], 0, s[48:49]
	v_add_co_u32_e32 v16, vcc, s65, v16
	s_nop 1
	v_addc_co_u32_e32 v17, vcc, 0, v17, vcc
	global_store_dwordx2 v[16:17], v[0:1], off offset:1024
	global_store_dwordx2 v[18:19], v[2:3], off offset:32
	global_store_dwordx2 v[18:19], v[4:5], off offset:64
	global_store_dwordx2 v[18:19], v[6:7], off offset:96
	global_store_dwordx2 v[18:19], v[8:9], off offset:128
	global_store_dwordx2 v[18:19], v[10:11], off offset:160
	global_store_dwordx2 v[18:19], v[12:13], off offset:192
	global_store_dwordx2 v[18:19], v[14:15], off offset:224

; template <int L> DI void layer_phases(const Params& P, Frame& F, const XcdBarrier& bar, int lo, int hi) {
;     ...
;             for (;;) {
;                 __syncthreads();
;                 if (F.tid == 0) F.MISC[24] = __hip_atomic_fetch_add(qctr, 1u, __ATOMIC_RELAXED, __HIP_MEMORY_SCOPE_AGENT);
;                 __syncthreads();
;                 const int u = (int)F.MISC[24];
.LBB0_2613:
	s_barrier
	s_and_saveexec_b64 s[6:7], s[4:5]
	s_cbranch_execz .LBB0_2617
	s_waitcnt vmcnt(0)
	v_mov_b32_e32 v1, s67
	ds_write_b32 v1, v252
